# g2 + phase G: token loop no longer drains the previous token's stores before starting the next token's loads
# speedup vs baseline: 1.0239x; 1.0006x over previous
.LBB0_2906:
	v_mov_b32_e32 v2, 0
	s_and_saveexec_b64 s[18:19], s[2:3]
	s_cbranch_execz .LBB0_2908
	s_waitcnt lgkmcnt(0)
	v_ashrrev_i32_e32 v2, 16, v59
	v_lshl_add_u32 v2, v2, 2, 0
	v_add_u32_e32 v2, 0x20420, v2
	ds_read_b32 v2, v2
	s_waitcnt lgkmcnt(0)
	v_add_u32_sdwa v2, v2, v59 dst_sel:DWORD dst_unused:UNUSED_PAD src0_sel:DWORD src1_sel:WORD_0
.LBB0_2908:
	s_or_b64 exec, exec, s[18:19]
	s_add_i32 s15, s4, s14
	s_cmpk_gt_i32 s15, 0x1fff
	s_cselect_b64 s[18:19], -1, 0
	s_cmpk_lt_i32 s15, 0x2000
	s_cselect_b64 s[20:21], -1, 0
	s_and_b64 s[22:23], s[20:21], s[2:3]
	s_waitcnt lgkmcnt(0)
	v_mov_b32_e32 v110, v1
	s_and_saveexec_b64 s[20:21], s[22:23]
	s_cbranch_execz .LBB0_2910
	v_lshl_or_b32 v4, s15, 3, v102
	v_ashrrev_i32_e32 v5, 31, v4
	v_lshlrev_b64 v[4:5], 2, v[4:5]
	v_lshl_add_u64 v[6:7], s[8:9], 0, v[4:5]
	v_lshl_add_u64 v[4:5], s[10:11], 0, v[4:5]
	flat_load_dword v59, v[6:7]
	flat_load_dword v110, v[4:5]

.LBB0_2913:
	v_cvt_pk_bf16_f32 v10, v10, v11
	v_cvt_pk_bf16_f32 v11, v12, v13
	v_cvt_pk_bf16_f32 v12, v6, v7
	v_cvt_pk_bf16_f32 v13, v8, v9
	global_store_dwordx4 v[32:33], v[10:13], off
